# v9 with 124 converter workgroups
# speedup vs baseline: 1.0116x; 1.0111x over previous
.LBB0_226:
	s_cmp_lt_i32 s28, 3
	s_cselect_b64 s[0:1], -1, 0
	s_cmp_gt_i32 s29, 2
	s_cselect_b64 s[6:7], -1, 0
	s_and_b64 s[0:1], s[0:1], s[6:7]
	s_andn2_b64 vcc, exec, s[0:1]
	s_cbranch_vccnz .LBB0_398
	s_cmpk_lg_i32 s33, 0x100
	s_cselect_b32 s3, s33, 0x7c
	s_sub_i32 s6, s33, s3
	s_cmp_lt_i32 s2, s6
	s_cselect_b64 s[0:1], -1, 0
	s_sub_i32 s30, s2, s6
	s_cmpk_gt_i32 s30, 0x2fff
	s_cselect_b64 s[6:7], -1, 0
	s_or_b64 s[0:1], s[0:1], s[6:7]
	v_lshrrev_b32_e32 v82, 5, v0
	v_lshlrev_b32_e32 v80, 4, v0
	v_lshrrev_b32_e32 v1, 7, v0
	v_lshrrev_b32_e32 v81, 3, v0
	s_and_b64 vcc, exec, s[0:1]
	s_cbranch_vccnz .LBB0_237
	v_readlane_b32 s6, v252, 0
	v_readlane_b32 s7, v252, 1
	v_readfirstlane_b32 s34, v0
	s_nop 4
	s_sub_u32 s6, s6, 0xe8
	s_subb_u32 s7, s7, 0
	s_load_dwordx2 s[8:9], s[6:7], 0xa8
	s_load_dwordx2 s[10:11], s[6:7], 0xb8
	s_lshr_b32 s34, s34, 6
	s_add_u32 s12, s26, 0x5800000
	s_addc_u32 s13, s27, 0
	s_add_u32 s14, s26, 0x25800000
	s_addc_u32 s15, s27, 0
	s_mov_b32 s35, 0xc3e00000
	v_mov_b32_e32 v160, 0x43e00000
	s_mov_b32 s31, 124
	s_sub_u32 s0, 0x2fff, s30
	s_mul_hi_u32 s41, s0, 0x2108422
	s_add_u32 s41, s41, 1
	v_and_b32_e32 v77, 63, v0
	v_and_b32_e32 v66, 31, v77
	v_lshlrev_b32_e32 v66, 4, v66
	v_lshrrev_b32_e32 v67, 5, v77
	v_lshlrev_b32_e32 v68, 4, v77
	v_lshl_add_u32 v69, v67, 9, v66
	s_lshr_b32 s0, s34, 1
	v_and_b32_e32 v78, 3, v77
	v_xor_b32_e32 v78, s0, v78
	v_and_b32_e32 v71, 4, v77
	v_or_b32_e32 v78, v78, v71
	v_lshlrev_b32_e32 v78, 4, v78
	s_and_b32 s0, s34, 1
	s_lshl_b32 s0, s0, 3
	v_lshl_or_b32 v71, v77, 9, s0
	v_or_b32_e32 v71, v71, v78
	v_xor_b32_e32 v72, 64, v71
	v_add_u32_e32 v73, 0x8000, v71
	v_add_u32_e32 v74, 0x8000, v72
	s_lshl_b32 s0, s34, 1
	v_add_u32_e32 v78, s0, v67
	v_xor_b32_e32 v78, v78, v77
	v_and_b32_e32 v78, 7, v78
	v_lshlrev_b32_e32 v78, 4, v78
	v_lshrrev_b32_e32 v75, 3, v77
	s_lshl_b32 s0, s34, 3
	v_add_u32_e32 v75, s0, v75
	v_and_b32_e32 v76, 7, v77
	v_lshlrev_b32_e32 v76, 4, v76
	v_lshl_add_u32 v76, v75, 11, v76
	v_lshl_add_u32 v75, v75, 7, v78
	s_waitcnt lgkmcnt(0)
	s_min_u32 s0, s30, 0x2fff
	s_add_u32 s30, s30, s31
	s_cmp_lt_u32 s0, 0x2000
	s_cbranch_scc0 .Lcv_w2_1
	s_lshr_b32 s1, s0, 8
	s_bfe_u32 s3, s0, 0x40004
	s_bfe_u32 s7, s0, 0x30001
	s_and_b32 s0, s0, 1
	s_lshl_b32 s6, s1, 25
	s_lshl_b32 s49, s3, 21
	s_add_u32 s6, s6, s49
	s_lshl_b32 s49, s34, 17
	s_add_u32 s6, s6, s49
	s_lshl_b32 s49, s0, 13
	s_add_u32 s6, s6, s49
	s_lshl_b32 s49, s7, 10
	s_add_u32 s6, s6, s49
	s_add_u32 s62, s8, s6
	s_addc_u32 s63, s9, 0
	s_lshl_b32 s6, s1, 23
	s_lshl_b32 s49, s7, 20
	s_add_u32 s6, s6, s49
	s_lshl_b32 s49, s0, 18
	s_add_u32 s6, s6, s49
	s_lshl_b32 s49, s3, 7
	s_add_u32 s6, s6, s49
	s_add_u32 s52, s12, s6
	s_addc_u32 s53, s13, 0
	s_mov_b32 s70, 0x4000
	s_mov_b32 s71, 0xe4000
	s_mov_b32 s86, 0x60000
	v_mov_b32_e32 v70, v68
	s_branch .Lcv_dec_done_1
